# lazy rescale made per-row (a row keeps its reference unless its own max grows by >16): result independent of which rows share a wave
# speedup vs baseline: 1.0062x; 1.0062x over previous
;     ...
;                 mx = fmaxf(mx, __shfl_xor(mx, 32));
;                 const float mnew = fmaxf(mrun, mx); const bool grew = __any(mnew > mrun);
;                 if (grew) {
;                     const float alpha = __builtin_amdgcn_exp2f((mrun - mnew) * L2E);
;                     ls0 *= alpha; ls1 *= alpha; ls2 *= alpha; ls3 *= alpha;
; #pragma unroll
;                     for (int i = 0; i < 16; ++i) { oacc[0][i] *= alpha; oacc[1][i] *= alpha; } }
;                 mrun = mnew;
.Lattn_resc:
	v_cndmask_b32_e32 v32, v202, v32, vcc
	v_sub_f32_e32 v33, v202, v32
	v_mul_f32_e32 v33, 0x3fb8aa3b, v33
	v_exp_f32_e32 v34, v33
	s_nop 0
	v_pk_mul_f32 v[30:31], v[30:31], v[34:35] op_sel_hi:[1,0]
	v_pk_mul_f32 v[28:29], v[28:29], v[34:35] op_sel_hi:[1,0]
	v_pk_mul_f32 v[26:27], v[26:27], v[34:35] op_sel_hi:[1,0]
	v_pk_mul_f32 v[24:25], v[24:25], v[34:35] op_sel_hi:[1,0]
	v_pk_mul_f32 v[22:23], v[22:23], v[34:35] op_sel_hi:[1,0]
	v_pk_mul_f32 v[20:21], v[20:21], v[34:35] op_sel_hi:[1,0]
	v_pk_mul_f32 v[18:19], v[18:19], v[34:35] op_sel_hi:[1,0]
	v_pk_mul_f32 v[16:17], v[16:17], v[34:35] op_sel_hi:[1,0]
	v_pk_mul_f32 v[14:15], v[14:15], v[34:35] op_sel_hi:[1,0]
	v_pk_mul_f32 v[12:13], v[12:13], v[34:35] op_sel_hi:[1,0]
	v_pk_mul_f32 v[10:11], v[10:11], v[34:35] op_sel_hi:[1,0]
	v_pk_mul_f32 v[8:9], v[8:9], v[34:35] op_sel_hi:[1,0]
	v_pk_mul_f32 v[6:7], v[6:7], v[34:35] op_sel_hi:[1,0]
	v_pk_mul_f32 v[4:5], v[4:5], v[34:35] op_sel_hi:[1,0]
	v_pk_mul_f32 v[2:3], v[2:3], v[34:35] op_sel_hi:[1,0]
	v_pk_mul_f32 v[0:1], v[0:1], v[34:35] op_sel_hi:[1,0]
	v_pk_mul_f32 v[120:121], v[120:121], v[34:35] op_sel_hi:[1,0]
	v_pk_mul_f32 v[118:119], v[118:119], v[34:35] op_sel_hi:[1,0]
